# ldsdma_1
# baseline (speedup 1.0000x reference)
_Z10gae_kernelPKfPKiS2_S0_S0_S0_PfS3_:
	s_load_dwordx8 s[4:11], s[0:1], 0x0
	s_load_dwordx4 s[12:15], s[0:1], 0x20
	v_and_b32_e32 v64, 63, v0
	v_lshrrev_b32_e32 v1, 6, v0
	s_andn2_b32 s16, s2, 63
	s_and_b32 s17, s2, 7
	s_lshl_b32 s17, s17, 3
	s_bfe_u32 s18, s2, 0x30003
	s_or_b32 s16, s16, s17
	s_or_b32 s2, s16, s18
	v_readfirstlane_b32 s20, v1
	s_mul_i32 s20, s20, 0x3000
	s_add_u32 s20, s20, 64
	v_lshlrev_b32_e32 v74, 4, v64
	v_add_u32_e32 v74, s20, v74
	s_mov_b32 s3, 0
	s_lshl_b64 s[2:3], s[2:3], 11
	v_lshlrev_b32_e32 v2, 9, v1
	v_lshlrev_b32_e32 v3, 2, v64
	v_or3_b32 v2, s2, v2, v3
	v_mov_b32_e32 v3, s3
	v_lshlrev_b64 v[18:19], 2, v[2:3]
	s_waitcnt lgkmcnt(0)
	v_lshl_add_u64 v[54:55], s[14:15], 0, v[18:19]
	v_lshl_add_u64 v[52:53], s[6:7], 0, v[18:19]
	s_add_u32 m0, s20, 0x2800
	s_nop 0
	global_load_lds_dwordx4 v[54:55], off nt
	s_add_u32 m0, s20, 0x800
	s_nop 0
	global_load_lds_dwordx4 v[52:53], off nt
	v_lshl_add_u64 v[56:57], s[8:9], 0, v[18:19]
	s_add_u32 m0, s20, 0x1000
	s_nop 0
	global_load_lds_dwordx4 v[56:57], off nt
	v_lshl_add_u64 v[58:59], s[12:13], 0, v[18:19]
	s_add_u32 m0, s20, 0x2000
	s_nop 0
	global_load_lds_dwordx4 v[58:59], off nt
	v_lshl_add_u64 v[60:61], s[4:5], 0, v[18:19]
	s_add_u32 m0, s20, 0x0
	s_nop 0
	global_load_lds_dwordx4 v[60:61], off nt
	v_lshl_add_u64 v[62:63], s[10:11], 0, v[18:19]
	s_add_u32 m0, s20, 0x1800
	s_nop 0
	global_load_lds_dwordx4 v[62:63], off nt
	s_add_u32 m0, s20, 0x0
	s_nop 0
	global_load_lds_dwordx4 v[60:61], off offset:1024 nt
	s_add_u32 m0, s20, 0x800
	s_nop 0
	global_load_lds_dwordx4 v[52:53], off offset:1024 nt
	s_add_u32 m0, s20, 0x1000
	s_nop 0
	global_load_lds_dwordx4 v[56:57], off offset:1024 nt
	s_add_u32 m0, s20, 0x1800
	s_nop 0
	global_load_lds_dwordx4 v[62:63], off offset:1024 nt
	s_add_u32 m0, s20, 0x2000
	s_nop 0
	global_load_lds_dwordx4 v[58:59], off offset:1024 nt
	s_add_u32 m0, s20, 0x2800
	s_nop 0
	global_load_lds_dwordx4 v[54:55], off offset:1024 nt
	v_mov_b32_e32 v66, 0
	v_mov_b32_e32 v68, 1.0
	v_mov_b32_e32 v69, 0
	v_mov_b32_e32 v70, 1.0
	v_mov_b32_e32 v71, 0
	v_mov_b32_e32 v72, 1.0
	v_bfe_u32 v73, v0, 4, 2
	v_cmp_gt_u32_e64 s[4:5], 16, v64
	v_mov_b32_e32 v65, 0
	v_mov_b32_e32 v67, 1.0
	s_waitcnt vmcnt(11)
	ds_read_b128 v[10:13], v74 offset:10240
	s_waitcnt lgkmcnt(0)
	v_mul_f32_e32 v12, 0x3f7d70a4, v12
	s_waitcnt vmcnt(10)
	ds_read_b128 v[14:17], v74 offset:2048
	s_waitcnt lgkmcnt(0)
	v_cmp_eq_u32_e32 vcc, 0, v14
	v_mul_f32_e32 v13, 0x3f7d70a4, v13
	v_mul_f32_e32 v10, 0x3f7d70a4, v10
	v_cndmask_b32_e64 v14, 0, 1.0, vcc
	s_waitcnt vmcnt(9)
	ds_read_b128 v[20:23], v74 offset:4096
	s_waitcnt lgkmcnt(0)
	v_cmp_eq_u32_e32 vcc, 0, v20
	v_mul_f32_e32 v11, 0x3f7d70a4, v11
	s_waitcnt vmcnt(8)
	ds_read_b128 v[24:27], v74 offset:8192
	s_waitcnt lgkmcnt(0)
	v_mul_f32_e32 v26, v26, v12
	v_cndmask_b32_e64 v20, 0, 1.0, vcc
	v_cmp_eq_u32_e32 vcc, 0, v15
	v_mul_f32_e32 v27, v27, v13
	v_mul_f32_e32 v24, v24, v10
	v_cndmask_b32_e64 v15, 0, 1.0, vcc
	v_cmp_eq_u32_e32 vcc, 0, v21
	v_mul_f32_e32 v25, v25, v11
	v_mul_f32_e32 v12, 0x3f733333, v12
	v_cndmask_b32_e64 v21, 0, 1.0, vcc
	v_cmp_eq_u32_e32 vcc, 0, v16
	v_mul_f32_e32 v13, 0x3f733333, v13
	v_mul_f32_e32 v10, 0x3f733333, v10
	v_cndmask_b32_e64 v16, 0, 1.0, vcc
	v_cmp_eq_u32_e32 vcc, 0, v22
	s_waitcnt vmcnt(7)
	ds_read_b128 v[28:31], v74 offset:0
	s_waitcnt lgkmcnt(0)
	v_fma_f32 v16, v26, v16, v30
	v_mul_f32_e32 v11, 0x3f733333, v11
	v_cndmask_b32_e64 v22, 0, 1.0, vcc
	v_cmp_eq_u32_e32 vcc, 0, v17
	v_fma_f32 v14, v24, v14, v28
	v_fma_f32 v15, v25, v15, v29
	v_cndmask_b32_e64 v17, 0, 1.0, vcc
	v_cmp_eq_u32_e32 vcc, 0, v23
	v_fmac_f32_e32 v31, v27, v17
	v_mul_f32_e32 v22, v12, v22
	v_cndmask_b32_e64 v23, 0, 1.0, vcc
	v_mul_f32_e32 v23, v13, v23
	s_waitcnt vmcnt(6)
	ds_read_b128 v[2:5], v74 offset:6144
	s_waitcnt lgkmcnt(0)
	v_sub_f32_e32 v12, v16, v4
	v_sub_f32_e32 v13, v31, v5
	v_mul_f32_e32 v20, v10, v20
	v_mul_f32_e32 v21, v11, v21
	v_sub_f32_e32 v10, v14, v2
	v_sub_f32_e32 v11, v15, v3
	v_mul_f32_e32 v14, v23, v22
	v_fma_f32 v15, v22, v13, v12
	v_mul_f32_e32 v14, v14, v21
	v_fma_f32 v15, v21, v15, v11
	v_mul_f32_e32 v14, v14, v20
	v_fma_f32 v24, v20, v15, v10
	v_mov_b32_e32 v16, 1.0
	v_mov_b32_dpp v68, v14 row_shl:1 row_mask:0xf bank_mask:0xf
	v_mov_b32_dpp v66, v24 row_shl:1 row_mask:0xf bank_mask:0xf
	v_mul_f32_e32 v15, v14, v68
	v_fmac_f32_e32 v24, v14, v66
	v_cmp_eq_u32_e32 vcc, 2, v73
	v_mov_b32_dpp v70, v15 row_shl:2 row_mask:0xf bank_mask:0xf
	v_mov_b32_dpp v69, v24 row_shl:2 row_mask:0xf bank_mask:0xf
	v_mul_f32_e32 v14, v15, v70
	v_fmac_f32_e32 v24, v15, v69
	v_mov_b32_e32 v15, 0
	v_mov_b32_dpp v72, v14 row_shl:4 row_mask:0xf bank_mask:0xf
	v_mov_b32_dpp v71, v24 row_shl:4 row_mask:0xf bank_mask:0xf
	v_fmac_f32_e32 v24, v14, v71
	v_mul_f32_e32 v14, v14, v72
	s_nop 0
	v_mov_b32_dpp v15, v24 row_shl:8 row_mask:0xf bank_mask:0xf
	v_mov_b32_dpp v16, v14 row_shl:8 row_mask:0xf bank_mask:0xf
	v_fmac_f32_e32 v24, v14, v15
	v_mul_f32_e32 v14, v14, v16
	v_readlane_b32 s9, v24, 32
	v_readlane_b32 s2, v14, 48
	v_readlane_b32 s8, v14, 32
	v_readlane_b32 s6, v14, 16
	v_mov_b32_e32 v15, s2
	v_mul_f32_e32 v16, s8, v15
	v_cndmask_b32_e32 v15, 1.0, v15, vcc
	v_cmp_eq_u32_e64 s[2:3], 1, v73
	v_readlane_b32 s10, v24, 48
	v_mul_f32_e32 v17, s6, v16
	v_cndmask_b32_e64 v15, v15, v16, s[2:3]
	v_readlane_b32 s7, v24, 16
	v_cndmask_b32_e64 v15, v15, v17, s[4:5]
	v_mov_b32_e32 v16, s9
	v_mov_b32_e32 v17, s10
	v_fmac_f32_e32 v16, s8, v17
	v_mov_b32_e32 v25, s7
	v_cndmask_b32_e32 v17, 0, v17, vcc
	v_fmac_f32_e32 v25, s6, v16
	v_cndmask_b32_e64 v16, v17, v16, s[2:3]
	v_cndmask_b32_e64 v16, v16, v25, s[4:5]
	s_waitcnt vmcnt(4)
	ds_read_b128 v[32:35], v74 offset:1024
	ds_read_b128 v[36:39], v74 offset:3072
	s_waitcnt lgkmcnt(0)
	v_cmp_eq_u32_e64 s[6:7], 0, v36
	v_fmac_f32_e32 v24, v14, v16
	v_mul_f32_e32 v28, v14, v15
	s_waitcnt vmcnt(0)
	ds_read_b128 v[40:43], v74 offset:5120
	ds_read_b128 v[6:9], v74 offset:7168
	ds_read_b128 v[44:47], v74 offset:9216
	ds_read_b128 v[48:51], v74 offset:11264
	s_waitcnt lgkmcnt(0)
	v_mul_f32_e32 v15, 0x3f7d70a4, v48
	v_cndmask_b32_e64 v14, 0, 1.0, s[6:7]
	v_cmp_eq_u32_e64 s[6:7], 0, v40
	v_mul_f32_e32 v17, v44, v15
	v_mul_f32_e32 v15, 0x3f733333, v15
	v_cndmask_b32_e64 v16, 0, 1.0, s[6:7]
	v_cmp_eq_u32_e64 s[6:7], 0, v37
	v_mul_f32_e32 v25, v15, v16
	v_mul_f32_e32 v16, 0x3f7d70a4, v49
	v_cndmask_b32_e64 v15, 0, 1.0, s[6:7]
	v_cmp_eq_u32_e64 s[6:7], 0, v41
	v_fma_f32 v14, v17, v14, v32
	v_mul_f32_e32 v26, v45, v16
	v_cndmask_b32_e64 v17, 0, 1.0, s[6:7]
	v_mul_f32_e32 v16, 0x3f733333, v16
	v_fma_f32 v15, v26, v15, v33
	v_mul_f32_e32 v26, v16, v17
	v_mul_f32_e32 v17, 0x3f7d70a4, v50
	v_cmp_eq_u32_e64 s[6:7], 0, v38
	v_mul_f32_e32 v29, v46, v17
	v_mul_f32_e32 v17, 0x3f733333, v17
	v_cndmask_b32_e64 v16, 0, 1.0, s[6:7]
	v_cmp_eq_u32_e64 s[6:7], 0, v42
	v_fma_f32 v16, v29, v16, v34
	v_mul_f32_e32 v29, 0x3f7d70a4, v51
	v_cndmask_b32_e64 v27, 0, 1.0, s[6:7]
	v_cmp_eq_u32_e64 s[6:7], 0, v39
	v_mul_f32_e32 v27, v17, v27
	v_mul_f32_e32 v31, v47, v29
	v_cndmask_b32_e64 v17, 0, 1.0, s[6:7]
	v_cmp_eq_u32_e64 s[6:7], 0, v43
	v_fmac_f32_e32 v35, v31, v17
	v_mul_f32_e32 v29, 0x3f733333, v29
	v_cndmask_b32_e64 v30, 0, 1.0, s[6:7]
	v_sub_f32_e32 v16, v16, v8
	v_sub_f32_e32 v17, v35, v9
	v_mul_f32_e32 v29, v29, v30
	v_sub_f32_e32 v15, v15, v7
	v_fma_f32 v30, v27, v17, v16
	v_mul_f32_e32 v31, v29, v27
	v_sub_f32_e32 v14, v14, v6
	v_fma_f32 v30, v26, v30, v15
	v_mul_f32_e32 v31, v31, v26
	v_fma_f32 v30, v25, v30, v14
	v_mul_f32_e32 v31, v31, v25
	v_mov_b32_e32 v32, 0
	v_mov_b32_e32 v33, 1.0
	s_nop 0
	v_mov_b32_dpp v32, v30 row_shl:1 row_mask:0xf bank_mask:0xf
	v_mov_b32_dpp v33, v31 row_shl:1 row_mask:0xf bank_mask:0xf
	v_fmac_f32_e32 v30, v31, v32
	v_mul_f32_e32 v31, v31, v33
	v_mov_b32_e32 v32, 0
	v_mov_b32_e32 v33, 1.0
	s_nop 0
	v_mov_b32_dpp v32, v30 row_shl:2 row_mask:0xf bank_mask:0xf
	v_mov_b32_dpp v33, v31 row_shl:2 row_mask:0xf bank_mask:0xf
	v_fmac_f32_e32 v30, v31, v32
	v_mul_f32_e32 v31, v31, v33
	v_mov_b32_e32 v32, 0
	v_mov_b32_e32 v33, 1.0
	s_nop 0
	v_mov_b32_dpp v32, v30 row_shl:4 row_mask:0xf bank_mask:0xf
	v_mov_b32_dpp v33, v31 row_shl:4 row_mask:0xf bank_mask:0xf
	v_fmac_f32_e32 v30, v31, v32
	v_mul_f32_e32 v31, v31, v33
	s_nop 0
	v_mov_b32_dpp v65, v30 row_shl:8 row_mask:0xf bank_mask:0xf
	v_mov_b32_dpp v67, v31 row_shl:8 row_mask:0xf bank_mask:0xf
	v_fmac_f32_e32 v30, v31, v65
	v_mul_f32_e32 v31, v31, v67
	v_readlane_b32 s9, v30, 32
	v_readlane_b32 s10, v31, 48
	v_readlane_b32 s8, v31, 32
	v_readlane_b32 s6, v31, 16
	v_mov_b32_e32 v32, s10
	v_mul_f32_e32 v33, s8, v32
	v_cndmask_b32_e32 v32, 1.0, v32, vcc
	v_readlane_b32 s11, v30, 48
	v_mul_f32_e32 v34, s6, v33
	v_cndmask_b32_e64 v32, v32, v33, s[2:3]
	v_readlane_b32 s7, v30, 16
	v_cndmask_b32_e64 v32, v32, v34, s[4:5]
	v_mov_b32_e32 v33, s9
	v_mov_b32_e32 v34, s11
	v_fmac_f32_e32 v33, s8, v34
	v_mov_b32_e32 v35, s7
	v_cndmask_b32_e32 v34, 0, v34, vcc
	v_fmac_f32_e32 v35, s6, v33
	v_cndmask_b32_e64 v33, v34, v33, s[2:3]
	v_cndmask_b32_e64 v33, v33, v35, s[4:5]
	v_fmac_f32_e32 v30, v31, v33
	v_mul_f32_e32 v31, v31, v32
	v_readlane_b32 s6, v28, 0
	v_readlane_b32 s7, v24, 0
	v_readlane_b32 s4, v31, 0
	v_readlane_b32 s5, v30, 0
	v_cmp_eq_u32_e32 vcc, 0, v64
	s_and_saveexec_b64 s[2:3], vcc
	s_cbranch_execz .LBB0_4
	v_mov_b32_e32 v32, s4
	v_mov_b32_e32 v33, s7
	v_mov_b32_e32 v34, s5
	v_mul_f32_e32 v32, s6, v32
	v_lshlrev_b32_e32 v1, 2, v1
	v_fmac_f32_e32 v33, s6, v34
	ds_write2_b32 v1, v32, v33 offset1:4
